# half unit (8 row loads) per wave per iteration, 18 units in attention, 6 in top-k, none left in phase 2
# baseline (speedup 1.0000x reference)
; #define LAS __attribute__((address_space(3)))
; __device__ __forceinline__ void convert_experts(Frame& F, int lo, int hi) {
;     const int gw = F.vcu * 8 + F.wave, NGW = F.G * 8;
;     LAS unsigned char* scr = F.lds + F.wave * 16384;
;     unsigned char* W1t = WSP(F, WS_W1T, unsigned char); unsigned char* W2t = WSP(F, WS_W2T, unsigned char);
;     const float* weg = F.a->in[I_WEG]; const float* weu = F.a->in[I_WEU]; const float* wed = F.a->in[I_WED];
;     const float* wsg = F.a->in[I_WSG]; const float* wsu = F.a->in[I_WSU]; const float* wsd = F.a->in[I_WSD];
;     ...
;     constexpr int NPAIRS = CONV_ITEMS / 2;
;     (void)lo; (void)hi;
;     ...
;     if (gw < NPAIRS) {
;         const int ns = 2 * ((NPAIRS - gw + NGW - 1) / NGW);
;         int sq = 0, r = CONV_RIDX(0);
;         TItem tc, tn; CONV_DESC(r, tc); tn = tc;
;         int p = 0; bool first = true;
.Lcva_vcu:
	s_lshr_b32 s99, s99, 6
	s_lshl_b32 s101, s101, 3
	s_add_u32 s89, s101, s99
	s_movk_i32 s90, 18
	s_mov_b32 s32, 0
	s_mov_b32 s95, 0
	s_mov_b32 s100, 0
	s_waitcnt vmcnt(0)
	s_branch .LBB0_304

; #define LAS __attribute__((address_space(3)))
; __device__ __forceinline__ void lds_barrier() { asm volatile("s_waitcnt lgkmcnt(0)\n\ts_barrier" ::: "memory"); }
; __device__ __forceinline__ void convert_experts(Frame& F, int lo, int hi) {
;     ...
;             const bool more = sq + 1 < ns; const int rn = more ? CONV_RIDX(sq + 1) : r;
;             if (more) { CONV_DESC(rn, tn); titem_issue(tn, F.lane, scr + (p ^ 1) * 8192); }
; __device__ __forceinline__ void phase_attn(Frame& F) {
;     ...
;         lds_barrier();
;         LAS unsigned char* kb = F.lds + buf * ABUF;
;         const bf16x8 q0 = qn0, q1 = qn1;
;         {
;             LAS unsigned char* ob = F.lds + (buf ^ 1) * ABUF;
; #pragma unroll
;             for (int jj = 0; jj < 4; ++jj) { const int ch = tid + 512 * jj, row = ch >> 3, c16 = ch & 7;
;                 *(LAS u32x4*)(ob + row * ATT_ROWB + c16 * 16) = kr[jj]; *(LAS u32x4*)(ob + ATT_VOFF + row * ATT_ROWB + c16 * 16) = vr[jj]; }
;         }
;         const AttnUnit nu = un;
;         un = attn_decode(x8 * PER_X + (jl + 2 * G8 < jlast ? jl + 2 * G8 : jlast)); attn_issue(qkv, un, tid, kr, vr);
;         { const char* qb = (const char*)qkv + (((size_t)nu.b * SEQ + nu.r) * NPROJ + nu.h * 64) * 2; const unsigned qo = __umul24((unsigned)(128 * nu.n + ql), (unsigned)nu.d * (NPROJ * 2)) + 16u * fq;
;           qn0 = *(const bf16x8*)(qb + qo); qn1 = *(const bf16x8*)(qb + qo + 64); }
;         const unsigned qrow = __umul24((unsigned)(128 * cu.n + ql), (unsigned)cu.d);
;         const float c1 = 0.125f * LOG2E;
;         const float nc2 = -__builtin_amdgcn_exp2f(-(float)(cu.h + 1)) * (float)cu.d * LOG2E;
;         const bool first = cu.n == 0;
;         f32x4 St[9];
;         const f32x4 eb = (f32x4){ef[0], ef[1], ef[2], ef[3]} * nc2;
;         float mx = -INFINITY;
;         bf16x8 kf[9][2];
; #pragma unroll
;         for (int T = 0; T < 9; ++T) { LAS unsigned char* ka = kb + (16 * (w + T) + fr) * ATT_ROWB + fq * 16; kf[T][0] = *(LAS bf16x8*)ka; kf[T][1] = *(LAS bf16x8*)(ka + 64); }
.Lcq_wd:
	v_mov_b64_e32 v[48:49], v[4:5]
	v_mov_b64_e32 v[46:47], v[2:3]
	v_mov_b64_e32 v[44:45], v[8:9]
	v_mov_b64_e32 v[42:43], v[6:7]
	s_lshl_b32 s65, 1, s35
	s_waitcnt lgkmcnt(0)
	s_barrier
	s_add_i32 s37, s30, 1
	v_cvt_f32_u32_e32 v54, s37
	v_cvt_f32_u32_e32 v55, s65
	v_add_u32_e32 v110, s85, v82
	v_add_u32_e32 v58, v110, v90
	v_exp_f32_e64 v54, -v54
	v_add_u32_e32 v66, v110, v91
	v_add_u32_e32 v74, v110, v92
	v_add_u32_e32 v111, v110, v93
	v_mul_f32_e32 v79, v55, v54
	ds_read_b128 v[54:57], v58
	ds_read_b128 v[58:61], v58 offset:64
	ds_read_b128 v[62:65], v66
	ds_read_b128 v[66:69], v66 offset:64
	ds_read_b128 v[70:73], v74
	ds_read_b128 v[74:77], v74 offset:64
	ds_read_b128 v[112:115], v111
	ds_read_b128 v[116:119], v111 offset:64
	v_add_u32_e32 v111, v110, v94
	ds_read_b128 v[120:123], v111
	ds_read_b128 v[124:127], v111 offset:64
	v_add_u32_e32 v111, v110, v95
	ds_read_b128 v[128:131], v111
	ds_read_b128 v[132:135], v111 offset:64
	v_add_u32_e32 v111, v110, v96
	ds_read_b128 v[136:139], v111
	ds_read_b128 v[140:143], v111 offset:64
	v_add_u32_e32 v111, v110, v97
	v_add_u32_e32 v110, v110, v98
	ds_read_b128 v[144:147], v111
	ds_read_b128 v[148:151], v111 offset:64
	ds_read_b128 v[152:155], v110
	ds_read_b128 v[156:159], v110 offset:64
	s_sub_u32 s32, s32, 1
	s_cmp_lt_i32 s32, 0
	s_cbranch_scc0 .Lcq_cont_l
	s_mov_b32 s32, 1
	s_mov_b32 s95, 0
	s_cmp_eq_u32 s90, 0
	s_cbranch_scc1 .Lcq_none_l
	s_sub_u32 s90, s90, 1
	s_lshr_b32 s98, s89, 6
	s_and_b32 s99, s89, 63
	s_mul_hi_u32 s100, s98, 0xaaaaaaab
	s_lshr_b32 s100, s100, 1
	s_mul_i32 s101, s100, 3
	s_sub_u32 s101, s98, s101
	s_cmp_lt_u32 s100, 256
	s_cselect_b32 s98, 0, 3
	s_cselect_b32 s95, s100, 0
	s_add_u32 s98, s98, s101
	s_lshl_b32 s98, s98, 1
	v_readlane_b32 s96, v253, s98
	s_add_u32 s98, s98, 1
	v_readlane_b32 s97, v253, s98
	s_lshl_b32 s95, s95, 20
	s_nop 3
	s_add_u32 s96, s96, s95
	s_addc_u32 s97, s97, 0
	s_cmp_eq_u32 s101, 2
	s_cbranch_scc1 .Lcq_down_l
	s_lshr_b32 s95, s99, 3
	s_and_b32 s99, s99, 7
	s_lshl_b32 s98, s95, 17
	s_add_u32 s96, s96, s98
	s_addc_u32 s97, s97, 0
	s_lshl_b32 s98, s99, 7
	s_add_u32 s96, s96, s98
	s_addc_u32 s97, s97, 0
	s_lshl_b32 s100, s100, 19
	s_lshr_b32 s98, s99, 2
	s_lshl_b32 s98, s98, 18
	s_add_u32 s100, s100, s98
	s_and_b32 s98, s99, 3
	s_lshl_b32 s98, s98, 15
	s_add_u32 s100, s100, s98
	s_lshl_b32 s98, s101, 17
	s_add_u32 s100, s100, s98
	s_lshl_b32 s98, s95, 7
	s_add_u32 s100, s100, s98
	v_readlane_b32 s92, v253, 12
	v_readlane_b32 s93, v253, 13
	s_mov_b32 s94, 0xc3317218
	s_cmp_eq_u32 s101, 0
	s_cselect_b32 s94, 0xc2b8aa3b, s94
	s_nop 3
	s_add_u32 s92, s92, s100
	s_addc_u32 s93, s93, 0
	s_movk_i32 s95, 0x400
	s_movk_i32 s98, 0x400
	s_branch .Lcq_go_l

; #define LAS __attribute__((address_space(3)))
; __device__ __forceinline__ void titem_issue(const TItem& t, int lane, LAS unsigned char* buf) {
;     const int nblk = t.N / 32, kb = t.item / nblk, nb = t.item % nblk, k0 = 64 * kb, n0 = 32 * nb;
; #pragma unroll
;     for (int j = 0; j < 8; ++j) { const float* g = t.W + (size_t)(k0 + 8 * j + (lane >> 3)) * t.N + n0 + 4 * ((lane & 7) ^ j);
;         __builtin_amdgcn_global_load_lds((const unsigned*)g, (LAS unsigned*)(buf + j * 1024), 16, 0, 2); }
; }
; __device__ __forceinline__ void phase_attn(Frame& F) {
;     ...
; #pragma unroll
;         for (int T = 0; T < 9; ++T) { LAS unsigned char* ka = kb + (16 * (w + T) + fr) * ATT_ROWB + fq * 16; kf[T][0] = *(LAS bf16x8*)ka; kf[T][1] = *(LAS bf16x8*)(ka + 64); }
;         __builtin_amdgcn_sched_barrier(0);
; #pragma unroll
;         for (int T = 0; T < 9; ++T) {
;             f32x4 sa = (f32x4){0.f, 0.f, 0.f, 0.f};
;             sa = __builtin_amdgcn_mfma_f32_16x16x32_bf16(kf[T][0], q0, sa, 0, 0, 0);
;             sa = __builtin_amdgcn_mfma_f32_16x16x32_bf16(kf[T][1], q1, sa, 0, 0, 0);
;             const float kT = (!first || w + T >= 8) ? nc2 * (float)(128 - 16 * T) : -INFINITY;
;             sa = sa * c1 + (eb + kT);
; #pragma unroll
;             for (int rg = 0; rg < 4; ++rg) {
;                 if (T == 0) sa[rg] = ef[rg] <= 0.f ? sa[rg] : -INFINITY;
;                 if (T == 8) sa[rg] = ef[rg] >= 0.f ? sa[rg] : -INFINITY;
;             }
;             St[T] = sa;
;             mx = fmaxf(mx, fmaxf(fmaxf(sa[0], sa[1]), fmaxf(sa[2], sa[3])));
;         }
.Lcq_cont_l:
	s_cmp_eq_u32 s95, 0
	s_cbranch_scc1 .Lcq_none_l
	s_lshl_b32 s99, s98, 4
	v_mad_u32_u24 v250, v248, s99, v249
	global_load_dwordx4 v[168:171], v250, s[96:97] nt
	s_add_u32 s96, s96, s98
	s_addc_u32 s97, s97, 0
	global_load_dwordx4 v[172:175], v250, s[96:97] nt
	s_add_u32 s96, s96, s98
	s_addc_u32 s97, s97, 0
	global_load_dwordx4 v[176:179], v250, s[96:97] nt
	s_add_u32 s96, s96, s98
	s_addc_u32 s97, s97, 0
	global_load_dwordx4 v[180:183], v250, s[96:97] nt
	s_add_u32 s96, s96, s98
	s_addc_u32 s97, s97, 0
	global_load_dwordx4 v[184:187], v250, s[96:97] nt
	s_add_u32 s96, s96, s98
	s_addc_u32 s97, s97, 0
	global_load_dwordx4 v[188:191], v250, s[96:97] nt
	s_add_u32 s96, s96, s98
	s_addc_u32 s97, s97, 0
	global_load_dwordx4 v[192:195], v250, s[96:97] nt
	s_add_u32 s96, s96, s98
	s_addc_u32 s97, s97, 0
	global_load_dwordx4 v[196:199], v250, s[96:97] nt
	s_add_u32 s96, s96, s98
	s_addc_u32 s97, s97, 0
.Lcq_none_l:
	s_cmp_lg_u32 s64, 0
	v_lshl_add_u32 v78, s64, 7, v86
	s_cselect_b64 s[64:65], -1, 0
	v_mul_f32_e32 v160, 0xbfb8aa3b, v79
	v_and_b32_e32 v110, 0xffffff, v78
	s_waitcnt lgkmcnt(14)
	v_mfma_f32_16x16x32_bf16 v[54:57], v[54:57], v[46:49], 0
	v_mul_f32_e32 v78, 0x43000000, v160
	s_or_b64 vcc, s[64:65], s[38:39]
	v_cndmask_b32_e32 v78, v109, v78, vcc
	v_mfma_f32_16x16x32_bf16 v[54:57], v[58:61], v[42:45], v[54:57]
	v_fma_f32 v162, v50, v160, v78
	v_fma_f32 v163, v51, v160, v78
	v_pk_fma_f32 v[78:79], v[52:53], v[160:161], v[78:79] op_sel_hi:[1,0,0]
	s_or_b64 vcc, s[64:65], s[40:41]
	s_nop 3
	v_pk_fma_f32 v[56:57], v[56:57], s[56:57], v[78:79] op_sel_hi:[1,0,1]
	v_pk_fma_f32 v[54:55], v[54:55], s[56:57], v[162:163] op_sel_hi:[1,0,1]
	v_cndmask_b32_e64 v164, v109, v56, s[10:11]
	v_cndmask_b32_e64 v162, v109, v54, s[6:7]
	v_cndmask_b32_e64 v163, v109, v55, s[8:9]
	v_cndmask_b32_e64 v165, v109, v57, s[12:13]
	v_mfma_f32_16x16x32_bf16 v[54:57], v[62:65], v[46:49], 0
	v_max_f32_e32 v58, v162, v163
	v_max_f32_e32 v59, v164, v165
	v_max3_f32 v62, v58, v59, s78
	v_mfma_f32_16x16x32_bf16 v[54:57], v[66:69], v[42:45], v[54:57]
	v_mul_f32_e32 v58, 0x42e00000, v160
	v_cndmask_b32_e32 v58, v109, v58, vcc
	v_pk_fma_f32 v[60:61], v[50:51], v[160:161], v[58:59] op_sel_hi:[1,0,0]
	v_pk_fma_f32 v[58:59], v[52:53], v[160:161], v[58:59] op_sel_hi:[1,0,0]
	s_or_b64 vcc, s[64:65], s[42:43]
	s_nop 2
	v_pk_fma_f32 v[166:167], v[56:57], s[56:57], v[58:59] op_sel_hi:[1,0,1]
	s_waitcnt lgkmcnt(13)
	v_mfma_f32_16x16x32_bf16 v[56:59], v[70:73], v[46:49], 0
	v_fma_f32 v78, v54, s56, v60
	v_fma_f32 v79, v55, s56, v61
	v_max_f32_e32 v54, v166, v167
	v_max3_f32 v63, v78, v79, v54
	s_waitcnt lgkmcnt(12)
	v_mfma_f32_16x16x32_bf16 v[54:57], v[74:77], v[42:45], v[56:59]
	s_nop 2
	v_mul_f32_e32 v58, 0x42c00000, v160
	v_cndmask_b32_e32 v58, v109, v58, vcc
	v_pk_fma_f32 v[60:61], v[50:51], v[160:161], v[58:59] op_sel_hi:[1,0,0]
	v_pk_fma_f32 v[58:59], v[52:53], v[160:161], v[58:59] op_sel_hi:[1,0,0]
	s_nop 0
	v_pk_fma_f32 v[76:77], v[54:55], s[56:57], v[60:61] op_sel_hi:[1,0,1]
	v_pk_fma_f32 v[74:75], v[56:57], s[56:57], v[58:59] op_sel_hi:[1,0,1]
	s_waitcnt lgkmcnt(11)
	v_mfma_f32_16x16x32_bf16 v[54:57], v[112:115], v[46:49], 0
	v_max_f32_e32 v58, v74, v75
	v_max3_f32 v58, v76, v77, v58
	v_max3_f32 v62, v62, v63, v58
	s_waitcnt lgkmcnt(10)
	v_mfma_f32_16x16x32_bf16 v[54:57], v[116:119], v[42:45], v[54:57]
	v_mul_f32_e32 v58, 0x42a00000, v160
	s_or_b64 vcc, s[64:65], s[44:45]
	v_cndmask_b32_e32 v58, v109, v58, vcc
	v_pk_fma_f32 v[60:61], v[50:51], v[160:161], v[58:59] op_sel_hi:[1,0,0]
	v_pk_fma_f32 v[58:59], v[52:53], v[160:161], v[58:59] op_sel_hi:[1,0,0]
	s_nop 2
	v_pk_fma_f32 v[72:73], v[54:55], s[56:57], v[60:61] op_sel_hi:[1,0,1]
	v_pk_fma_f32 v[70:71], v[56:57], s[56:57], v[58:59] op_sel_hi:[1,0,1]
	s_waitcnt lgkmcnt(9)
	v_mfma_f32_16x16x32_bf16 v[56:59], v[120:123], v[46:49], 0
	v_max_f32_e32 v54, v70, v71
	v_max3_f32 v63, v72, v73, v54
	s_or_b64 vcc, s[64:65], s[46:47]
	s_waitcnt lgkmcnt(8)
	v_mfma_f32_16x16x32_bf16 v[54:57], v[124:127], v[42:45], v[56:59]
	s_nop 2
	v_mul_f32_e32 v58, 0x42800000, v160
	v_cndmask_b32_e32 v58, v109, v58, vcc
	v_pk_fma_f32 v[60:61], v[50:51], v[160:161], v[58:59] op_sel_hi:[1,0,0]
	v_pk_fma_f32 v[58:59], v[52:53], v[160:161], v[58:59] op_sel_hi:[1,0,0]
	s_nop 0
	v_pk_fma_f32 v[68:69], v[54:55], s[56:57], v[60:61] op_sel_hi:[1,0,1]
	v_pk_fma_f32 v[66:67], v[56:57], s[56:57], v[58:59] op_sel_hi:[1,0,1]
	s_waitcnt lgkmcnt(7)
	v_mfma_f32_16x16x32_bf16 v[54:57], v[128:131], v[46:49], 0
	v_max_f32_e32 v58, v66, v67
	v_max3_f32 v58, v68, v69, v58
	v_max3_f32 v111, v62, v63, v58
	s_waitcnt lgkmcnt(6)
	v_mfma_f32_16x16x32_bf16 v[54:57], v[132:135], v[42:45], v[54:57]
	v_mul_f32_e32 v58, 0x42400000, v160
	s_or_b64 vcc, s[64:65], s[48:49]
	v_cndmask_b32_e32 v58, v109, v58, vcc
	v_pk_fma_f32 v[60:61], v[50:51], v[160:161], v[58:59] op_sel_hi:[1,0,0]
	v_pk_fma_f32 v[58:59], v[52:53], v[160:161], v[58:59] op_sel_hi:[1,0,0]
	s_nop 2
	v_pk_fma_f32 v[64:65], v[54:55], s[56:57], v[60:61] op_sel_hi:[1,0,1]
	v_pk_fma_f32 v[62:63], v[56:57], s[56:57], v[58:59] op_sel_hi:[1,0,1]
	s_waitcnt lgkmcnt(5)
	v_mfma_f32_16x16x32_bf16 v[56:59], v[136:139], v[46:49], 0
	v_max_f32_e32 v54, v62, v63
	v_max3_f32 v112, v64, v65, v54
	s_or_b64 vcc, s[64:65], s[50:51]
	s_waitcnt lgkmcnt(4)
	v_mfma_f32_16x16x32_bf16 v[54:57], v[140:143], v[42:45], v[56:59]
	s_nop 2
	v_mul_f32_e32 v58, 0x42000000, v160
	v_cndmask_b32_e32 v58, v109, v58, vcc
	v_pk_fma_f32 v[60:61], v[50:51], v[160:161], v[58:59] op_sel_hi:[1,0,0]
	v_pk_fma_f32 v[58:59], v[52:53], v[160:161], v[58:59] op_sel_hi:[1,0,0]
	s_nop 0
	v_pk_fma_f32 v[60:61], v[54:55], s[56:57], v[60:61] op_sel_hi:[1,0,1]
	v_pk_fma_f32 v[58:59], v[56:57], s[56:57], v[58:59] op_sel_hi:[1,0,1]
	s_waitcnt lgkmcnt(3)
; __device__ __forceinline__ void phase_attn(Frame& F) {
;     ...
;             LAS unsigned char* ob = F.lds + (buf ^ 1) * ABUF;
; #pragma unroll
;             for (int jj = 0; jj < 4; ++jj) { const int ch = tid + 512 * jj, row = ch >> 3, c16 = ch & 7;
;                 *(LAS u32x4*)(ob + row * ATT_ROWB + c16 * 16) = kr[jj]; *(LAS u32x4*)(ob + ATT_VOFF + row * ATT_ROWB + c16 * 16) = vr[jj]; }
;         }
;         const AttnUnit nu = un;
;         un = attn_decode(x8 * PER_X + (jl + 2 * G8 < jlast ? jl + 2 * G8 : jlast)); attn_issue(qkv, un, tid, kr, vr);
;         { const char* qb = (const char*)qkv + (((size_t)nu.b * SEQ + nu.r) * NPROJ + nu.h * 64) * 2; const unsigned qo = __umul24((unsigned)(128 * nu.n + ql), (unsigned)nu.d * (NPROJ * 2)) + 16u * fq;
;           qn0 = *(const bf16x8*)(qb + qo); qn1 = *(const bf16x8*)(qb + qo + 64); }
;         const unsigned qrow = __umul24((unsigned)(128 * cu.n + ql), (unsigned)cu.d);
;         const float c1 = 0.125f * LOG2E;
;         const float nc2 = -__builtin_amdgcn_exp2f(-(float)(cu.h + 1)) * (float)cu.d * LOG2E;
;         const bool first = cu.n == 0;
;         f32x4 St[9];
;         const f32x4 eb = (f32x4){ef[0], ef[1], ef[2], ef[3]} * nc2;
;         float mx = -INFINITY;
;         bf16x8 kf[9][2];
; #pragma unroll
;         for (int T = 0; T < 9; ++T) { LAS unsigned char* ka = kb + (16 * (w + T) + fr) * ATT_ROWB + fq * 16; kf[T][0] = *(LAS bf16x8*)ka; kf[T][1] = *(LAS bf16x8*)(ka + 64); }
;         __builtin_amdgcn_sched_barrier(0);
; #pragma unroll
;         for (int T = 0; T < 9; ++T) {
;             f32x4 sa = (f32x4){0.f, 0.f, 0.f, 0.f};
;             sa = __builtin_amdgcn_mfma_f32_16x16x32_bf16(kf[T][0], q0, sa, 0, 0, 0);
;             sa = __builtin_amdgcn_mfma_f32_16x16x32_bf16(kf[T][1], q1, sa, 0, 0, 0);
;             const float kT = (!first || w + T >= 8) ? nc2 * (float)(128 - 16 * T) : -INFINITY;
;             sa = sa * c1 + (eb + kT);
; #pragma unroll
;             for (int rg = 0; rg < 4; ++rg) {
;                 if (T == 0) sa[rg] = ef[rg] <= 0.f ? sa[rg] : -INFINITY;
;                 if (T == 8) sa[rg] = ef[rg] >= 0.f ? sa[rg] : -INFINITY;
;             }
;             St[T] = sa;
;             mx = fmaxf(mx, fmaxf(fmaxf(sa[0], sa[1]), fmaxf(sa[2], sa[3])));
;         }
;         mx = fmaxf(mx, __shfl_xor(mx, 16)); mx = fmaxf(mx, __shfl_xor(mx, 32));
;         f32x4 lv = (f32x4){0.f, 0.f, 0.f, 0.f};
	v_mfma_f32_16x16x32_bf16 v[54:57], v[144:147], v[46:49], 0
	v_max_f32_e32 v113, v58, v59
	v_max3_f32 v113, v60, v61, v113
	v_max3_f32 v111, v111, v112, v113
	s_waitcnt lgkmcnt(1)
	v_mfma_f32_16x16x32_bf16 v[46:49], v[152:155], v[46:49], 0
	s_or_b64 vcc, s[64:65], s[52:53]
	v_add_u32_e32 v144, s85, v89
	v_add_u32_e32 v130, v144, v99
	v_mfma_f32_16x16x32_bf16 v[112:115], v[148:151], v[42:45], v[54:57]
	v_add_u32_e32 v140, v144, v100
	v_add_u32_e32 v145, v144, v101
	s_nop 0
	v_mul_f32_e32 v54, 0x41800000, v160
	s_waitcnt lgkmcnt(0)
	v_mfma_f32_16x16x32_bf16 v[42:45], v[156:159], v[42:45], v[46:49]
	s_add_i32 s37, s77, s70
	s_xor_b32 s79, s79, 1
	s_min_i32 s37, s37, s71
	s_mul_i32 s58, s79, 0x12000
	s_add_i32 s37, s37, s3
	v_add_u32_e32 v2, s58, v84
	s_mul_hi_i32 s58, s37, 0x2aaaaaab
	s_lshr_b32 s59, s58, 31
	s_ashr_i32 s58, s58, 4
	s_add_i32 s59, s58, s59
	s_mul_i32 s58, s59, 0x60
	s_sub_i32 s37, s37, s58
	s_ashr_i32 s58, s59, 3
	s_and_b32 s80, s59, 7
	v_add_u32_e32 v3, v2, v83
	s_cmp_gt_i32 s37, 31
	ds_write_b128 v3, v[38:41]
	ds_write_b128 v3, v[34:37] offset:36864
	v_add_u32_e32 v3, v2, v85
	s_cselect_b64 s[82:83], -1, 0
	s_cmp_gt_i32 s37, 63
	ds_write_b128 v3, v[30:33]
	ds_write_b128 v3, v[26:29] offset:36864
	v_add_u32_e32 v3, v2, v87
	v_add_u32_e32 v2, v2, v88
	s_cselect_b64 s[86:87], -1, 0
	ds_write_b128 v3, v[22:25]
	ds_write_b128 v3, v[18:21] offset:36864
	ds_write_b128 v2, v[14:17]
	ds_write_b128 v2, v[10:13] offset:36864
	v_cndmask_b32_e64 v2, 0, 1, s[86:87]
	s_cmp_lg_u64 s[82:83], 0
	v_readfirstlane_b32 s59, v2
	s_addc_u32 s81, s59, 0
	s_lshl_b32 s59, s81, 5
	s_lshl_b32 s82, s81, 1
	s_sub_i32 s37, s37, s59
	s_sub_i32 s59, 5, s82
	s_ashr_i32 s83, s37, s59
	s_lshl_b32 s59, -1, s59
	s_andn2_b32 s84, s37, s59
	s_ashr_i32 s59, s58, 31
	s_lshl_b64 s[86:87], s[58:59], 12
	s_ashr_i32 s37, s83, 31
	s_add_u32 s59, s86, s83
	s_addc_u32 s37, s87, s37
	s_mulk_i32 s37, 0xa00
	s_mul_hi_u32 s86, s59, 0xa00
	s_add_i32 s87, s86, s37
	s_mulk_i32 s59, 0xa00
	s_lshl_b32 s37, s80, 6
	s_or_b32 s86, s59, s37
	s_lshl_b64 s[86:87], s[86:87], 1
	s_add_u32 s37, s33, s86
	s_addc_u32 s59, s66, s87
	s_add_u32 s86, s37, 0x400
	s_addc_u32 s87, s59, 0
	s_lshl_b32 s59, s84, 7
	v_add_u32_e32 v2, s59, v81
	s_lshl_b32 s37, 0x1400, s82
	v_max_i32_e32 v3, 0, v2
	v_mul_u32_u24_e32 v3, s37, v3
	v_or_b32_e32 v3, v3, v80
	global_load_dwordx4 v[38:41], v3, s[86:87]
	global_load_dwordx4 v[34:37], v3, s[86:87] offset:1024
	v_max_i32_e32 v3, 0xffffffc0, v2
	v_add_u32_e32 v3, 64, v3
	v_mul_u32_u24_e32 v3, s37, v3
	v_or_b32_e32 v3, v3, v80
	global_load_dwordx4 v[30:33], v3, s[86:87]
	global_load_dwordx4 v[26:29], v3, s[86:87] offset:1024
	v_add_u32_e32 v3, s59, v1
	v_max_i32_e32 v2, 0xffffff40, v2
	v_max_i32_e32 v3, 0, v3
	v_add_u32_e32 v2, 0xc0, v2
	v_mul_u32_u24_e32 v3, s37, v3
	v_mul_u32_u24_e32 v2, s37, v2
	v_or_b32_e32 v3, v3, v80
	v_or_b32_e32 v2, v2, v80
	s_ashr_i32 s37, s36, 31
	global_load_dwordx4 v[22:25], v3, s[86:87]
	global_load_dwordx4 v[18:21], v3, s[86:87] offset:1024
	global_load_dwordx4 v[14:17], v2, s[86:87]
	global_load_dwordx4 v[10:13], v2, s[86:87] offset:1024
	s_lshl_b64 s[86:87], s[36:37], 12
	s_ashr_i32 s37, s73, 31
	s_add_u32 s59, s86, s73
	s_addc_u32 s37, s87, s37
	s_mulk_i32 s37, 0xa00
	s_mul_hi_u32 s86, s59, 0xa00
	s_add_i32 s87, s86, s37
	s_mulk_i32 s59, 0xa00
	s_lshl_b32 s37, s75, 6
	s_or_b32 s86, s59, s37
	s_lshl_b64 s[86:87], s[86:87], 1
	s_add_u32 s86, s33, s86
	s_addc_u32 s87, s66, s87
	s_lshl_b32 s37, 0x1400, s74
	v_lshl_add_u32 v2, s76, 7, v86
	s_and_b32 s37, s37, 0x555400
	v_mul_u32_u24_e32 v2, s37, v2
	v_or_b32_e32 v6, v2, v82
	global_load_dwordx4 v[2:5], v6, s[86:87]
	s_nop 0
	global_load_dwordx4 v[6:9], v6, s[86:87] offset:64
	v_cndmask_b32_e32 v54, v109, v54, vcc
	s_or_b64 vcc, s[64:65], s[54:55]
	v_pk_fma_f32 v[56:57], v[50:51], v[160:161], v[54:55] op_sel_hi:[1,0,0]
	v_mul_f32_e32 v46, 0, v160
	v_cndmask_b32_e32 v46, v109, v46, vcc
	v_pk_fma_f32 v[48:49], v[50:51], v[160:161], v[46:47] op_sel_hi:[1,0,0]
	v_pk_fma_f32 v[46:47], v[52:53], v[160:161], v[46:47] op_sel_hi:[1,0,0]
	v_pk_fma_f32 v[54:55], v[52:53], v[160:161], v[54:55] op_sel_hi:[1,0,0]
	v_pk_fma_f32 v[44:45], v[44:45], s[56:57], v[46:47] op_sel_hi:[1,0,1]
	v_pk_fma_f32 v[42:43], v[42:43], s[56:57], v[48:49] op_sel_hi:[1,0,1]
	v_cndmask_b32_e64 v48, v109, v44, s[18:19]
	v_and_b32_e32 v44, 64, v108
	v_pk_fma_f32 v[54:55], v[114:115], s[56:57], v[54:55] op_sel_hi:[1,0,1]
	v_cndmask_b32_e64 v47, v109, v43, s[16:17]
	v_cndmask_b32_e64 v49, v109, v45, s[20:21]
	v_xor_b32_e32 v43, 16, v108
	v_add_u32_e32 v44, 64, v44
	v_pk_fma_f32 v[56:57], v[112:113], s[56:57], v[56:57] op_sel_hi:[1,0,1]
	v_max_f32_e32 v112, v54, v55
	v_cndmask_b32_e64 v46, v109, v42, s[14:15]
	v_max_f32_e32 v42, v48, v49
	v_cmp_lt_i32_e32 vcc, v43, v44
	v_max3_f32 v112, v56, v57, v112
	v_max3_f32 v42, v46, v47, v42
	v_cndmask_b32_e32 v43, v108, v43, vcc
	v_max3_f32 v42, v111, v112, v42
	v_lshlrev_b32_e32 v142, 2, v43
	ds_bpermute_b32 v43, v142, v42
	s_waitcnt lgkmcnt(0)
	v_max_f32_e32 v43, v43, v43
	v_max_f32_e32 v42, v42, v43
	v_xor_b32_e32 v43, 32, v108
	v_cmp_lt_i32_e32 vcc, v43, v44
	s_nop 1
	v_cndmask_b32_e32 v43, v108, v43, vcc
	v_lshlrev_b32_e32 v143, 2, v43
	ds_bpermute_b32 v43, v143, v42
	s_waitcnt lgkmcnt(0)
; #define LAS __attribute__((address_space(3)))
; __device__ __forceinline__ unsigned cvt_pk_bf16(float lo, float hi) { const f32x2_t v = {lo, hi}; return __builtin_bit_cast(unsigned, __builtin_convertvector(v, bf16x2_t)); }
; __device__ __forceinline__ float fast_exp2(float x) { return __builtin_amdgcn_exp2f(x); }
; __device__ __forceinline__ s16x4 tr_read(LAS unsigned char* p) { return __builtin_bit_cast(s16x4, __builtin_amdgcn_ds_read_tr16_b64_v4i16((LAS s16x4*)p)); }
; __device__ __forceinline__ void phase_attn(Frame& F) {
;     ...
;         f32x4 lv = (f32x4){0.f, 0.f, 0.f, 0.f};
;         f32x4 nmx = (f32x4){-mx, -mx, -mx, -mx}; asm volatile("" : "+v"(nmx));
; #pragma unroll
;         for (int T = 0; T < 9; ++T) { const f32x4 d = St[T] + nmx; f32x4 pv; pv.x = fast_exp2(d.x); pv.y = fast_exp2(d.y); pv.z = fast_exp2(d.z); pv.w = fast_exp2(d.w); St[T] = pv; lv = lv + pv; }
;         float l = (lv.x + lv.y) + (lv.z + lv.w);
;         l += __shfl_xor(l, 16); l += __shfl_xor(l, 32);
;         f32x4 O[4];
; #pragma unroll
;         for (int dt = 0; dt < 4; ++dt) O[dt] = (f32x4){0.f, 0.f, 0.f, 0.f};
; #pragma unroll
;         for (int T = 0; T < 9; ++T) {
;             u32x2 pw; pw.x = cvt_pk_bf16(St[T][0], St[T][1]); pw.y = cvt_pk_bf16(St[T][2], St[T][3]);
;             const s16x4 pb = __builtin_bit_cast(s16x4, pw);
;             LAS unsigned char* va = kb + ATT_VOFF + (16 * (w + T) + 4 * fq + (fr >> 2)) * ATT_ROWB + (8 * (fr & 3)) * 2;
; #pragma unroll
;             for (int dt = 0; dt < 4; ++dt) O[dt] = __builtin_amdgcn_mfma_f32_16x16x16bf16_1k(tr_read(va + 64 * (dt >> 1) + 8 * (dt & 1)), pb, O[dt], 0, 0, 0);
;         }
	v_max_f32_e32 v43, v43, v43
	v_max_f32_e32 v111, v42, v43
	v_xor_b32_e32 v42, 0x80000000, v111
	v_mov_b32_e32 v43, v42
	v_mov_b32_e32 v44, v42
	v_mov_b32_e32 v45, v42
	ds_read_b64_tr_b16 v[120:121], v130 offset:36864
	v_pk_add_f32 v[118:119], v[166:167], v[44:45]
	v_pk_add_f32 v[112:113], v[164:165], v[44:45]
	v_exp_f32_e32 v126, v118
	v_exp_f32_e32 v127, v119
	ds_read_b64_tr_b16 v[118:119], v130 offset:36872
	v_pk_add_f32 v[114:115], v[162:163], v[42:43]
	v_exp_f32_e32 v112, v112
	v_exp_f32_e32 v114, v114
	v_exp_f32_e32 v113, v113
	v_exp_f32_e32 v115, v115
	ds_read_b64_tr_b16 v[128:129], v130 offset:36928
	ds_read_b64_tr_b16 v[130:131], v130 offset:36936
	v_pk_add_f32 v[134:135], v[76:77], v[42:43]
	v_cvt_pk_bf16_f32 v123, v112, v113
	v_cvt_pk_bf16_f32 v122, v114, v115
	v_pk_add_f32 v[116:117], v[112:113], 0 op_sel_hi:[1,0]
	v_pk_add_f32 v[124:125], v[114:115], 0 op_sel_hi:[1,0]
	s_waitcnt lgkmcnt(3)
	v_mfma_f32_16x16x16_bf16 v[112:115], v[120:121], v[122:123], 0
	v_add_f32_e64 v120, v74, v44
	v_add_f32_e64 v121, v75, v45
	v_pk_add_f32 v[132:133], v[126:127], v[116:117]
	v_exp_f32_e32 v136, v120
	s_waitcnt lgkmcnt(2)
	v_mfma_f32_16x16x16_bf16 v[116:119], v[118:119], v[122:123], 0
	v_exp_f32_e32 v137, v121
	v_pk_add_f32 v[78:79], v[78:79], v[42:43]
	v_cvt_pk_bf16_f32 v139, v126, v127
	s_waitcnt lgkmcnt(1)
	v_mfma_f32_16x16x16_bf16 v[74:77], v[128:129], v[122:123], 0
	ds_read_b64_tr_b16 v[128:129], v140 offset:36864
	v_exp_f32_e32 v78, v78
	v_exp_f32_e32 v79, v79
	s_waitcnt lgkmcnt(1)
	v_mfma_f32_16x16x16_bf16 v[120:123], v[130:131], v[122:123], 0
	ds_read_b64_tr_b16 v[130:131], v140 offset:36872
	ds_read_b64_tr_b16 v[126:127], v140 offset:36928
	ds_read_b64_tr_b16 v[140:141], v140 offset:36936
	v_cvt_pk_bf16_f32 v138, v78, v79
	v_exp_f32_e32 v134, v134
	v_exp_f32_e32 v135, v135
	s_waitcnt lgkmcnt(3)
	v_mfma_f32_16x16x16_bf16 v[112:115], v[128:129], v[138:139], v[112:115]
	v_add_f32_e64 v128, v70, v44
	v_add_f32_e64 v129, v71, v45
	v_pk_add_f32 v[78:79], v[78:79], v[124:125]
	v_pk_add_f32 v[124:125], v[136:137], v[132:133]
	s_waitcnt lgkmcnt(2)
	v_mfma_f32_16x16x16_bf16 v[116:119], v[130:131], v[138:139], v[116:119]
	v_add_f32_e64 v130, v72, v42
	v_add_f32_e64 v131, v73, v43
	v_pk_add_f32 v[78:79], v[134:135], v[78:79]
	v_exp_f32_e32 v128, v128
	s_waitcnt lgkmcnt(1)
	v_mfma_f32_16x16x16_bf16 v[70:73], v[126:127], v[138:139], v[74:77]
	ds_read_b64_tr_b16 v[126:127], v145 offset:36864
	v_exp_f32_e32 v129, v129
	v_pk_add_f32 v[48:49], v[44:45], v[48:49]
	s_waitcnt lgkmcnt(1)
	v_mfma_f32_16x16x16_bf16 v[74:77], v[140:141], v[138:139], v[120:123]
	v_add_f32_e64 v124, v128, v124
	v_add_f32_e64 v125, v129, v125
	s_nop 0
	ds_read_b64_tr_b16 v[120:121], v145 offset:36872
	v_cvt_pk_bf16_f32 v122, v134, v135
	ds_read_b64_tr_b16 v[132:133], v145 offset:36928
	ds_read_b64_tr_b16 v[134:135], v145 offset:36936
	v_cvt_pk_bf16_f32 v123, v136, v137
	v_add_u32_e32 v136, v144, v102
	s_waitcnt lgkmcnt(3)
	v_mfma_f32_16x16x16_bf16 v[112:115], v[126:127], v[122:123], v[112:115]
	v_exp_f32_e32 v126, v130
	v_exp_f32_e32 v127, v131
	v_pk_add_f32 v[130:131], v[68:69], v[42:43]
	s_waitcnt lgkmcnt(2)
	v_mfma_f32_16x16x16_bf16 v[116:119], v[120:121], v[122:123], v[116:119]
	v_add_f32_e64 v120, v66, v44
	v_add_f32_e64 v121, v67, v45
	v_pk_add_f32 v[78:79], v[126:127], v[78:79]
	v_exp_f32_e32 v130, v130
	s_waitcnt lgkmcnt(1)
	v_mfma_f32_16x16x16_bf16 v[66:69], v[132:133], v[122:123], v[70:73]
	ds_read_b64_tr_b16 v[132:133], v136 offset:36864
	v_exp_f32_e32 v120, v120
	v_exp_f32_e32 v121, v121
	s_waitcnt lgkmcnt(1)
	v_mfma_f32_16x16x16_bf16 v[70:73], v[134:135], v[122:123], v[74:77]
	ds_read_b64_tr_b16 v[122:123], v136 offset:36872
	v_cvt_pk_bf16_f32 v134, v126, v127
	v_cvt_pk_bf16_f32 v135, v128, v129
	ds_read_b64_tr_b16 v[128:129], v136 offset:36928
	ds_read_b64_tr_b16 v[136:137], v136 offset:36936
	s_waitcnt lgkmcnt(3)
	v_mfma_f32_16x16x16_bf16 v[74:77], v[132:133], v[134:135], v[112:115]
	v_add_u32_e32 v132, v144, v103
	ds_read_b64_tr_b16 v[126:127], v132 offset:36872
	v_exp_f32_e32 v131, v131
	s_waitcnt lgkmcnt(3)
	v_mfma_f32_16x16x16_bf16 v[112:115], v[122:123], v[134:135], v[116:119]
	ds_read_b64_tr_b16 v[122:123], v132 offset:36864
	v_pk_add_f32 v[124:125], v[120:121], v[124:125]
	v_pk_add_f32 v[78:79], v[130:131], v[78:79]
	v_pk_add_f32 v[116:117], v[62:63], v[44:45]
	v_pk_add_f32 v[118:119], v[64:65], v[42:43]
	s_waitcnt lgkmcnt(3)
	v_mfma_f32_16x16x16_bf16 v[62:65], v[128:129], v[134:135], v[66:69]
	v_exp_f32_e32 v116, v116
	v_exp_f32_e32 v117, v117
	v_cvt_pk_bf16_f32 v128, v130, v131
	v_cvt_pk_bf16_f32 v129, v120, v121
	ds_read_b64_tr_b16 v[120:121], v132 offset:36928
	ds_read_b64_tr_b16 v[130:131], v132 offset:36936
	v_add_u32_e32 v132, v144, v104
	s_waitcnt lgkmcnt(4)
	v_mfma_f32_16x16x16_bf16 v[66:69], v[136:137], v[134:135], v[70:73]
	v_exp_f32_e32 v118, v118
	v_exp_f32_e32 v119, v119
	s_waitcnt lgkmcnt(2)
	v_mfma_f32_16x16x16_bf16 v[70:73], v[122:123], v[128:129], v[74:77]
	v_add_f32_e64 v122, v116, v124
	v_add_f32_e64 v123, v117, v125
	ds_read_b64_tr_b16 v[124:125], v132 offset:36872
	v_pk_add_f32 v[78:79], v[118:119], v[78:79]
	v_mfma_f32_16x16x16_bf16 v[74:77], v[126:127], v[128:129], v[112:115]
	v_cvt_pk_bf16_f32 v127, v116, v117
	v_cvt_pk_bf16_f32 v126, v118, v119
	s_nop 0
	v_pk_add_f32 v[112:113], v[58:59], v[44:45]
	v_pk_add_f32 v[114:115], v[60:61], v[42:43]
	s_waitcnt lgkmcnt(2)
	v_mfma_f32_16x16x16_bf16 v[58:61], v[120:121], v[128:129], v[62:65]
	ds_read_b64_tr_b16 v[120:121], v132 offset:36864
	v_exp_f32_e32 v112, v112
	v_exp_f32_e32 v113, v113
	v_exp_f32_e32 v114, v114
	s_waitcnt lgkmcnt(2)
; #define LAS __attribute__((address_space(3)))
; __device__ __forceinline__ void titem_finish(const TItem& t, int lane, const LAS unsigned char* buf) {
;     ...
;     const float wsc = t.scale;
; #pragma unroll
;     for (int j = 0; j < 4; ++j) { const int n = (lane >> 3) + 8 * j; const LAS float* s = sb + (8 * c) * 32 + 4 * ((n >> 2) ^ c) + (n & 3);
; #pragma unroll
;         for (int q = 0; q < 8; ++q) v[j][q] = s[32 * q] * wsc; }
;     if (t.f8) {
; #pragma unroll
;         for (int j = 0; j < 4; ++j) { const int n = (lane >> 3) + 8 * j;
;             int w0 = __builtin_amdgcn_cvt_pk_fp8_f32(v[j][0], v[j][1], 0, false); w0 = __builtin_amdgcn_cvt_pk_fp8_f32(v[j][2], v[j][3], w0, true);
;             int w1 = __builtin_amdgcn_cvt_pk_fp8_f32(v[j][4], v[j][5], 0, false); w1 = __builtin_amdgcn_cvt_pk_fp8_f32(v[j][6], v[j][7], w1, true);
;             u32x2 o; o.x = (unsigned)w0; o.y = (unsigned)w1;
;             __builtin_nontemporal_store(o, (u32x2*)((unsigned char*)t.WT + (size_t)(d0 + n) * t.K + k0 + 8 * c)); }
; __device__ __forceinline__ void phase_attn(Frame& F) {
;     ...
;         for (int T = 0; T < 9; ++T) {
;             u32x2 pw; pw.x = cvt_pk_bf16(St[T][0], St[T][1]); pw.y = cvt_pk_bf16(St[T][2], St[T][3]);
;             const s16x4 pb = __builtin_bit_cast(s16x4, pw);
;             LAS unsigned char* va = kb + ATT_VOFF + (16 * (w + T) + 4 * fq + (fr >> 2)) * ATT_ROWB + (8 * (fr & 3)) * 2;
; #pragma unroll
;             for (int dt = 0; dt < 4; ++dt) O[dt] = __builtin_amdgcn_mfma_f32_16x16x16bf16_1k(tr_read(va + 64 * (dt >> 1) + 8 * (dt & 1)), pb, O[dt], 0, 0, 0);
;         }
;         const float inv = 1.f / l;
;         bf16_t* op = (bf16_t*)((char*)part + (((size_t)cu.dsel * NTOK + (size_t)cu.b * SEQ + cu.r) * 512 + cu.h * 64) * 2 + (qrow * 1024u + 16u * fq));
; #pragma unroll
;         for (int u2 = 0; u2 < 2; ++u2) { u32x4 o4; o4.x = cvt_pk_bf16(O[2 * u2][0] * inv, O[2 * u2][1] * inv); o4.y = cvt_pk_bf16(O[2 * u2][2] * inv, O[2 * u2][3] * inv);
;             o4.z = cvt_pk_bf16(O[2 * u2 + 1][0] * inv, O[2 * u2 + 1][1] * inv); o4.w = cvt_pk_bf16(O[2 * u2 + 1][2] * inv, O[2 * u2 + 1][3] * inv); *(u32x4*)(op + 32 * u2) = o4; }
;         if (fq == 0) *(float*)((char*)lse + (((size_t)cu.dsel * NTOK + (size_t)cu.b * SEQ + cu.r) * 8 + cu.h) * 4 + qrow * 32u) = mx + __builtin_amdgcn_logf(l);
	v_mfma_f32_16x16x16_bf16 v[62:65], v[130:131], v[128:129], v[66:69]
	ds_read_b64_tr_b16 v[116:117], v132 offset:36928
	ds_read_b64_tr_b16 v[128:129], v132 offset:36936
	v_exp_f32_e32 v115, v115
	v_pk_add_f32 v[118:119], v[112:113], v[122:123]
	v_add_u32_e32 v122, v144, v105
	s_waitcnt lgkmcnt(2)
	v_mfma_f32_16x16x16_bf16 v[66:69], v[120:121], v[126:127], v[70:73]
	ds_read_b64_tr_b16 v[120:121], v122 offset:36872
	v_mfma_f32_16x16x16_bf16 v[70:73], v[124:125], v[126:127], v[74:77]
	s_nop 2
	v_add_f32_e64 v74, v114, v78
	v_add_f32_e64 v75, v115, v79
	v_pk_add_f32 v[76:77], v[54:55], v[44:45]
	v_pk_add_f32 v[78:79], v[56:57], v[42:43]
	s_waitcnt lgkmcnt(2)
	v_mfma_f32_16x16x16_bf16 v[54:57], v[116:117], v[126:127], v[58:61]
	ds_read_b64_tr_b16 v[116:117], v122 offset:36864
	v_cvt_pk_bf16_f32 v114, v114, v115
	v_cvt_pk_bf16_f32 v115, v112, v113
	ds_read_b64_tr_b16 v[112:113], v122 offset:36928
	ds_read_b64_tr_b16 v[122:123], v122 offset:36936
	s_waitcnt lgkmcnt(4)
	v_mfma_f32_16x16x16_bf16 v[58:61], v[128:129], v[126:127], v[62:65]
	v_exp_f32_e32 v76, v76
	v_exp_f32_e32 v77, v77
	v_exp_f32_e32 v78, v78
	s_waitcnt lgkmcnt(2)
	v_mfma_f32_16x16x16_bf16 v[62:65], v[116:117], v[114:115], v[66:69]
	v_exp_f32_e32 v79, v79
	v_pk_add_f32 v[116:117], v[76:77], v[118:119]
	v_mfma_f32_16x16x16_bf16 v[66:69], v[120:121], v[114:115], v[70:73]
	s_nop 2
	v_add_f32_e64 v70, v42, v46
	v_add_f32_e64 v71, v43, v47
	s_waitcnt lgkmcnt(1)
	v_mfma_f32_16x16x16_bf16 v[42:45], v[112:113], v[114:115], v[54:57]
	v_exp_f32_e32 v72, v48
	v_exp_f32_e32 v73, v49
	v_exp_f32_e32 v70, v70
	v_add_u32_e32 v56, v144, v106
	ds_read_b64_tr_b16 v[54:55], v56 offset:36864
	s_waitcnt lgkmcnt(1)
	v_mfma_f32_16x16x16_bf16 v[46:49], v[122:123], v[114:115], v[58:61]
	v_exp_f32_e32 v71, v71
	v_cvt_pk_bf16_f32 v112, v78, v79
	v_cvt_pk_bf16_f32 v113, v76, v77
	ds_read_b64_tr_b16 v[58:59], v56 offset:36872
	ds_read_b64_tr_b16 v[76:77], v56 offset:36928
	ds_read_b64_tr_b16 v[114:115], v56 offset:36936
	s_waitcnt lgkmcnt(3)
	v_mfma_f32_16x16x16_bf16 v[54:57], v[54:55], v[112:113], v[62:65]
	s_nop 2
	v_add_f32_e64 v62, v78, v74
	v_add_f32_e64 v63, v79, v75
	v_pk_add_f32 v[64:65], v[72:73], v[116:117]
	v_pk_add_f32 v[62:63], v[70:71], v[62:63]
	v_add_u32_e32 v74, v144, v107
	s_waitcnt lgkmcnt(2)
	v_mfma_f32_16x16x16_bf16 v[58:61], v[58:59], v[112:113], v[66:69]
	s_nop 2
	v_pk_mov_b32 v[66:67], v[62:63], v[64:65] op_sel:[1,0]
	v_mov_b32_e32 v63, v65
	ds_read_b64_tr_b16 v[64:65], v74 offset:36864
	v_pk_add_f32 v[62:63], v[66:67], v[62:63]
	v_cvt_pk_bf16_f32 v66, v70, v71
	v_add_f32_e32 v75, v62, v63
	v_cvt_pk_bf16_f32 v67, v72, v73
	s_waitcnt lgkmcnt(2)
	v_mfma_f32_16x16x16_bf16 v[42:45], v[76:77], v[112:113], v[42:45]
	ds_read_b64_tr_b16 v[62:63], v74 offset:36872
	ds_read_b64_tr_b16 v[68:69], v74 offset:36928
	ds_read_b64_tr_b16 v[70:71], v74 offset:36936
	s_waitcnt lgkmcnt(3)
	v_mfma_f32_16x16x16_bf16 v[54:57], v[64:65], v[66:67], v[54:57]
	ds_bpermute_b32 v64, v142, v75
	s_waitcnt lgkmcnt(0)
	v_add_f32_e32 v72, v75, v64
	ds_bpermute_b32 v73, v143, v72
	v_mfma_f32_16x16x16_bf16 v[58:61], v[62:63], v[66:67], v[58:61]
	v_mfma_f32_16x16x16_bf16 v[62:65], v[68:69], v[66:67], v[42:45]
	s_waitcnt lgkmcnt(0)
	s_nop 1
	v_add_f32_e32 v43, v72, v73
	v_div_scale_f32 v68, s[64:65], v43, v43, 1.0
	v_mfma_f32_16x16x16_bf16 v[46:49], v[114:115], v[112:113], v[46:49]
	v_rcp_f32_e32 v69, v68
	v_lshlrev_b32_e32 v42, s35, v110
	s_ashr_i32 s35, s34, 31
	v_mfma_f32_16x16x16_bf16 v[44:47], v[70:71], v[66:67], v[46:49]
	s_lshl_b64 s[64:65], s[26:27], 16
	s_lshl_b64 s[34:35], s[34:35], 12
	s_ashr_i32 s26, s31, 31
	s_nop 0
	v_fma_f32 v48, -v68, v69, 1.0
	v_fmac_f32_e32 v69, v48, v69
	v_div_scale_f32 v48, vcc, 1.0, v43, 1.0
	v_mul_f32_e32 v49, v48, v69
	s_add_u32 s31, s34, s31
	v_fma_f32 v66, -v68, v49, v48
	s_addc_u32 s26, s35, s26
	v_fmac_f32_e32 v49, v66, v69
	s_add_u32 s34, s31, s64
	v_fma_f32 v48, -v68, v49, v48
	s_addc_u32 s35, s26, s65
	v_div_fmas_f32 v48, v48, v69, v49
	s_lshl_b32 s26, s30, 7
	s_lshl_b64 s[64:65], s[34:35], 10
	v_div_fixup_f32 v48, v48, v43, 1.0
	s_add_u32 s31, s24, s64
	v_lshl_or_b32 v49, v42, 10, v82
	s_addc_u32 s37, s25, s65
	v_pk_mul_f32 v[54:55], v[48:49], v[54:55] op_sel_hi:[0,1]
	v_pk_mul_f32 v[56:57], v[48:49], v[56:57] op_sel_hi:[0,1]
	s_add_u32 s64, s31, s26
	v_cvt_pk_bf16_f32 v54, v54, v55
	v_cvt_pk_bf16_f32 v55, v56, v57
	v_pk_mul_f32 v[56:57], v[48:49], v[58:59] op_sel_hi:[0,1]
	v_pk_mul_f32 v[58:59], v[48:49], v[60:61] op_sel_hi:[0,1]
	s_addc_u32 s65, s37, 0
	v_cvt_pk_bf16_f32 v56, v56, v57
	v_cvt_pk_bf16_f32 v57, v58, v59
	global_store_dwordx4 v49, v[54:57], s[64:65]
	v_pk_mul_f32 v[44:45], v[48:49], v[44:45] op_sel_hi:[0,1]
	s_nop 0
	v_pk_mul_f32 v[54:55], v[48:49], v[62:63] op_sel_hi:[0,1]
	v_pk_mul_f32 v[56:57], v[48:49], v[64:65] op_sel_hi:[0,1]
	v_cvt_pk_bf16_f32 v54, v54, v55
	v_cvt_pk_bf16_f32 v55, v56, v57
	v_cvt_pk_bf16_f32 v56, v44, v45
	v_pk_mul_f32 v[44:45], v[48:49], v[46:47] op_sel_hi:[0,1]
	v_cvt_pk_bf16_f32 v57, v44, v45
	global_store_dwordx4 v49, v[54:57], s[64:65] offset:64
	s_cmp_eq_u32 s95, 0
	s_cbranch_scc1 .Lcq_skip_l
	s_waitcnt vmcnt(12)
	v_pk_mul_f32 v[168:169], v[168:169], s[94:95] op_sel_hi:[1,0]
	v_pk_mul_f32 v[170:171], v[170:171], s[94:95] op_sel_hi:[1,0]
	v_pk_mul_f32 v[172:173], v[172:173], s[94:95] op_sel_hi:[1,0]
	v_pk_mul_f32 v[174:175], v[174:175], s[94:95] op_sel_hi:[1,0]
	v_pk_mul_f32 v[176:177], v[176:177], s[94:95] op_sel_hi:[1,0]
	v_pk_mul_f32 v[178:179], v[178:179], s[94:95] op_sel_hi:[1,0]
	v_pk_mul_f32 v[180:181], v[180:181], s[94:95] op_sel_hi:[1,0]
	v_pk_mul_f32 v[182:183], v[182:183], s[94:95] op_sel_hi:[1,0]
	v_pk_mul_f32 v[184:185], v[184:185], s[94:95] op_sel_hi:[1,0]
	v_pk_mul_f32 v[186:187], v[186:187], s[94:95] op_sel_hi:[1,0]
	v_pk_mul_f32 v[188:189], v[188:189], s[94:95] op_sel_hi:[1,0]
	v_pk_mul_f32 v[190:191], v[190:191], s[94:95] op_sel_hi:[1,0]
	v_pk_mul_f32 v[192:193], v[192:193], s[94:95] op_sel_hi:[1,0]
	v_pk_mul_f32 v[194:195], v[194:195], s[94:95] op_sel_hi:[1,0]
	v_pk_mul_f32 v[196:197], v[196:197], s[94:95] op_sel_hi:[1,0]
	v_pk_mul_f32 v[198:199], v[198:199], s[94:95] op_sel_hi:[1,0]
	s_cmp_eq_u32 s32, 1
	s_cbranch_scc0 .Lcq_q1_l
	v_cvt_pk_fp8_f32 v232, v168, v172
	v_cvt_pk_fp8_f32 v236, v169, v173
	v_cvt_pk_fp8_f32 v240, v170, v174
	v_cvt_pk_fp8_f32 v244, v171, v175
	v_cvt_pk_fp8_f32 v233, v184, v188
	v_cvt_pk_fp8_f32 v237, v185, v189
	v_cvt_pk_fp8_f32 v241, v186, v190
	v_cvt_pk_fp8_f32 v245, v187, v191
	v_cvt_pk_fp8_f32 v232, v176, v180 op_sel:[0,0,1]
	v_cvt_pk_fp8_f32 v236, v177, v181 op_sel:[0,0,1]
	v_cvt_pk_fp8_f32 v240, v178, v182 op_sel:[0,0,1]
	v_cvt_pk_fp8_f32 v244, v179, v183 op_sel:[0,0,1]
	v_cvt_pk_fp8_f32 v233, v192, v196 op_sel:[0,0,1]
	v_cvt_pk_fp8_f32 v237, v193, v197 op_sel:[0,0,1]
	v_cvt_pk_fp8_f32 v241, v194, v198 op_sel:[0,0,1]
	v_cvt_pk_fp8_f32 v245, v195, v199 op_sel:[0,0,1]
	s_branch .Lcq_skip_l
; __device__ __forceinline__ void titem_finish(const TItem& t, int lane, const LAS unsigned char* buf) {
;     ...
;     if (t.f8) {
; #pragma unroll
;         for (int j = 0; j < 4; ++j) { const int n = (lane >> 3) + 8 * j;
;             int w0 = __builtin_amdgcn_cvt_pk_fp8_f32(v[j][0], v[j][1], 0, false); w0 = __builtin_amdgcn_cvt_pk_fp8_f32(v[j][2], v[j][3], w0, true);
;             int w1 = __builtin_amdgcn_cvt_pk_fp8_f32(v[j][4], v[j][5], 0, false); w1 = __builtin_amdgcn_cvt_pk_fp8_f32(v[j][6], v[j][7], w1, true);
;             u32x2 o; o.x = (unsigned)w0; o.y = (unsigned)w1;
;             __builtin_nontemporal_store(o, (u32x2*)((unsigned char*)t.WT + (size_t)(d0 + n) * t.K + k0 + 8 * c)); }
.Lcq_q1_l:
	v_cvt_pk_fp8_f32 v234, v168, v172
	v_cvt_pk_fp8_f32 v238, v169, v173
	v_cvt_pk_fp8_f32 v242, v170, v174
	v_cvt_pk_fp8_f32 v246, v171, v175
	v_cvt_pk_fp8_f32 v235, v184, v188
	v_cvt_pk_fp8_f32 v239, v185, v189
	v_cvt_pk_fp8_f32 v243, v186, v190
	v_cvt_pk_fp8_f32 v247, v187, v191
	v_cvt_pk_fp8_f32 v234, v176, v180 op_sel:[0,0,1]
	v_cvt_pk_fp8_f32 v238, v177, v181 op_sel:[0,0,1]
	v_cvt_pk_fp8_f32 v242, v178, v182 op_sel:[0,0,1]
	v_cvt_pk_fp8_f32 v246, v179, v183 op_sel:[0,0,1]
	v_cvt_pk_fp8_f32 v235, v192, v196 op_sel:[0,0,1]
	v_cvt_pk_fp8_f32 v239, v193, v197 op_sel:[0,0,1]
	v_cvt_pk_fp8_f32 v243, v194, v198 op_sel:[0,0,1]
	v_cvt_pk_fp8_f32 v247, v195, v199 op_sel:[0,0,1]
	s_lshr_b32 s99, s95, 2
	v_lshlrev_b32_e32 v250, 4, v248
	v_mad_u32_u24 v250, v249, s99, v250
	v_add_u32_e32 v251, s95, v250
	v_add_u32_e32 v254, s95, v251
	v_add_u32_e32 v255, s95, v254
	global_store_dwordx4 v250, v[232:235], s[92:93] nt
	global_store_dwordx4 v251, v[236:239], s[92:93] nt
	global_store_dwordx4 v254, v[240:243], s[92:93] nt
	global_store_dwordx4 v255, v[244:247], s[92:93] nt
	s_mov_b32 s100, 1

; __device__ __forceinline__ void convert_experts(Frame& F, int lo, int hi) {
;     ...
;         for (;;) {
;             const bool more = sq + 1 < ns; const int rn = more ? CONV_RIDX(sq + 1) : r;
;             if (more) { CONV_DESC(rn, tn); titem_issue(tn, F.lane, scr + (p ^ 1) * 8192); }
;             if (!more) asm volatile("s_waitcnt vmcnt(0)" ::: "memory");
;             else if (first) asm volatile("s_waitcnt vmcnt(8)" ::: "memory");
;             else asm volatile("s_waitcnt vmcnt(12)" ::: "memory");
;             titem_finish(tc, F.lane, scr + p * 8192);
;             asm volatile("s_waitcnt lgkmcnt(0)" ::: "memory");
;             if (!more) break;
;             tc = tn; r = rn; ++sq; p ^= 1; first = false;
;         }
.Lcq_tail:
	s_sub_u32 s32, s32, 1
	s_cmp_lt_i32 s32, 0
	s_cbranch_scc0 .Lcq_cont_t
	s_mov_b32 s32, 1
	s_mov_b32 s95, 0
	s_cmp_eq_u32 s90, 0
	s_cbranch_scc1 .Lcq_none_t
	s_sub_u32 s90, s90, 1
	s_lshr_b32 s98, s89, 6
	s_and_b32 s99, s89, 63
	s_mul_hi_u32 s100, s98, 0xaaaaaaab
	s_lshr_b32 s100, s100, 1
	s_mul_i32 s101, s100, 3
	s_sub_u32 s101, s98, s101
	s_cmp_lt_u32 s100, 256
	s_cselect_b32 s98, 0, 3
	s_cselect_b32 s95, s100, 0
	s_add_u32 s98, s98, s101
	s_lshl_b32 s98, s98, 1
	v_readlane_b32 s96, v253, s98
	s_add_u32 s98, s98, 1
	v_readlane_b32 s97, v253, s98
	s_lshl_b32 s95, s95, 20
	s_nop 3
	s_add_u32 s96, s96, s95
	s_addc_u32 s97, s97, 0
	s_cmp_eq_u32 s101, 2
	s_cbranch_scc1 .Lcq_down_t
	s_lshr_b32 s95, s99, 3
	s_and_b32 s99, s99, 7
	s_lshl_b32 s98, s95, 17
	s_add_u32 s96, s96, s98
	s_addc_u32 s97, s97, 0
	s_lshl_b32 s98, s99, 7
	s_add_u32 s96, s96, s98
	s_addc_u32 s97, s97, 0
	s_lshl_b32 s100, s100, 19
	s_lshr_b32 s98, s99, 2
	s_lshl_b32 s98, s98, 18
	s_add_u32 s100, s100, s98
	s_and_b32 s98, s99, 3
	s_lshl_b32 s98, s98, 15
	s_add_u32 s100, s100, s98
	s_lshl_b32 s98, s101, 17
	s_add_u32 s100, s100, s98
	s_lshl_b32 s98, s95, 7
	s_add_u32 s100, s100, s98
	v_readlane_b32 s92, v253, 12
	v_readlane_b32 s93, v253, 13
	s_mov_b32 s94, 0xc3317218
	s_cmp_eq_u32 s101, 0
	s_cselect_b32 s94, 0xc2b8aa3b, s94
	s_nop 3
	s_add_u32 s92, s92, s100
	s_addc_u32 s93, s93, 0
	s_movk_i32 s95, 0x400
	s_movk_i32 s98, 0x400
	s_branch .Lcq_go_t

; #define LAS __attribute__((address_space(3)))
; __device__ __forceinline__ void titem_finish(const TItem& t, int lane, const LAS unsigned char* buf) {
;     ...
;     const float wsc = t.scale;
; #pragma unroll
;     for (int j = 0; j < 4; ++j) { const int n = (lane >> 3) + 8 * j; const LAS float* s = sb + (8 * c) * 32 + 4 * ((n >> 2) ^ c) + (n & 3);
; #pragma unroll
;         for (int q = 0; q < 8; ++q) v[j][q] = s[32 * q] * wsc; }
;     if (t.f8) {
; #pragma unroll
;         for (int j = 0; j < 4; ++j) { const int n = (lane >> 3) + 8 * j;
;             int w0 = __builtin_amdgcn_cvt_pk_fp8_f32(v[j][0], v[j][1], 0, false); w0 = __builtin_amdgcn_cvt_pk_fp8_f32(v[j][2], v[j][3], w0, true);
;             int w1 = __builtin_amdgcn_cvt_pk_fp8_f32(v[j][4], v[j][5], 0, false); w1 = __builtin_amdgcn_cvt_pk_fp8_f32(v[j][6], v[j][7], w1, true);
;             u32x2 o; o.x = (unsigned)w0; o.y = (unsigned)w1;
;             __builtin_nontemporal_store(o, (u32x2*)((unsigned char*)t.WT + (size_t)(d0 + n) * t.K + k0 + 8 * c)); }
.Lcq_none_t:
	s_cmp_eq_u32 s95, 0
	s_cbranch_scc1 .Lcq_tail_done
	s_waitcnt vmcnt(0)
	s_cmp_eq_u32 s95, 0
	s_cbranch_scc1 .Lcq_skip_t
	s_waitcnt vmcnt(0)
	v_pk_mul_f32 v[168:169], v[168:169], s[94:95] op_sel_hi:[1,0]
	v_pk_mul_f32 v[170:171], v[170:171], s[94:95] op_sel_hi:[1,0]
	v_pk_mul_f32 v[172:173], v[172:173], s[94:95] op_sel_hi:[1,0]
	v_pk_mul_f32 v[174:175], v[174:175], s[94:95] op_sel_hi:[1,0]
	v_pk_mul_f32 v[176:177], v[176:177], s[94:95] op_sel_hi:[1,0]
	v_pk_mul_f32 v[178:179], v[178:179], s[94:95] op_sel_hi:[1,0]
	v_pk_mul_f32 v[180:181], v[180:181], s[94:95] op_sel_hi:[1,0]
	v_pk_mul_f32 v[182:183], v[182:183], s[94:95] op_sel_hi:[1,0]
	v_pk_mul_f32 v[184:185], v[184:185], s[94:95] op_sel_hi:[1,0]
	v_pk_mul_f32 v[186:187], v[186:187], s[94:95] op_sel_hi:[1,0]
	v_pk_mul_f32 v[188:189], v[188:189], s[94:95] op_sel_hi:[1,0]
	v_pk_mul_f32 v[190:191], v[190:191], s[94:95] op_sel_hi:[1,0]
	v_pk_mul_f32 v[192:193], v[192:193], s[94:95] op_sel_hi:[1,0]
	v_pk_mul_f32 v[194:195], v[194:195], s[94:95] op_sel_hi:[1,0]
	v_pk_mul_f32 v[196:197], v[196:197], s[94:95] op_sel_hi:[1,0]
	v_pk_mul_f32 v[198:199], v[198:199], s[94:95] op_sel_hi:[1,0]
	s_cmp_eq_u32 s32, 1
	s_cbranch_scc0 .Lcq_q1_t
	v_cvt_pk_fp8_f32 v232, v168, v172
	v_cvt_pk_fp8_f32 v236, v169, v173
	v_cvt_pk_fp8_f32 v240, v170, v174
	v_cvt_pk_fp8_f32 v244, v171, v175
	v_cvt_pk_fp8_f32 v233, v184, v188
	v_cvt_pk_fp8_f32 v237, v185, v189
	v_cvt_pk_fp8_f32 v241, v186, v190
	v_cvt_pk_fp8_f32 v245, v187, v191
	v_cvt_pk_fp8_f32 v232, v176, v180 op_sel:[0,0,1]
	v_cvt_pk_fp8_f32 v236, v177, v181 op_sel:[0,0,1]
	v_cvt_pk_fp8_f32 v240, v178, v182 op_sel:[0,0,1]
	v_cvt_pk_fp8_f32 v244, v179, v183 op_sel:[0,0,1]
	v_cvt_pk_fp8_f32 v233, v192, v196 op_sel:[0,0,1]
	v_cvt_pk_fp8_f32 v237, v193, v197 op_sel:[0,0,1]
	v_cvt_pk_fp8_f32 v241, v194, v198 op_sel:[0,0,1]
	v_cvt_pk_fp8_f32 v245, v195, v199 op_sel:[0,0,1]
	s_branch .Lcq_skip_t

; #define LAS __attribute__((address_space(3)))
; __device__ __forceinline__ void convert_experts(Frame& F, int lo, int hi) {
;     const int gw = F.vcu * 8 + F.wave, NGW = F.G * 8;
;     LAS unsigned char* scr = F.lds + F.wave * 16384;
;     unsigned char* W1t = WSP(F, WS_W1T, unsigned char); unsigned char* W2t = WSP(F, WS_W2T, unsigned char);
;     const float* weg = F.a->in[I_WEG]; const float* weu = F.a->in[I_WEU]; const float* wed = F.a->in[I_WED];
;     const float* wsg = F.a->in[I_WSG]; const float* wsu = F.a->in[I_WSU]; const float* wsd = F.a->in[I_WSD];
;     ...
;     constexpr int NPAIRS = CONV_ITEMS / 2;
;     (void)lo; (void)hi;
;     ...
;     if (gw < NPAIRS) {
;         const int ns = 2 * ((NPAIRS - gw + NGW - 1) / NGW);
;         int sq = 0, r = CONV_RIDX(0);
; __device__ __forceinline__ void router_topk(Frame& F, int tile) {
;     const float* logits = WSP(F, WS_B, float); const float* br = F.a->in[I_BR];
;     int* tk_e = WSP(F, WS_TOPK_E, int); float* tk_g = WSP(F, WS_TOPK_G, float); int* tk_p = WSP(F, WS_TOPK_P, int);
;     int* gcnt = (int*)(F.a->ws + WS_CTL + CTL_CNT);
;     LAS int* hist = (LAS int*)F.lds; LAS int* base = hist + 256;
;     const int lane = F.lane, w = F.wave;
;     if (F.tid < 256) hist[F.tid] = 0;
;     __syncthreads();
;     const f32x4 bias = *(const f32x4*)(br + 4 * lane);
;     f32x4 lgn = *(const f32x4*)(logits + (size_t)(tile * 256 + w * 32) * 256 + 4 * lane);
;     int pe = 0, pp = 0; float pg = 0.f;
;     int* dumpi = (int*)(F.a->ws + WS_B + ((size_t)128 << 20));
.Lcvt_vcu:
	s_add_u32 s69, s41, s40
	s_and_b32 s69, s69, 3
	s_lshl_b32 s41, s41, 3
	s_add_u32 s89, s41, s40
	s_lshl_b32 s71, s64, 3
	s_mul_i32 s39, s71, 18
	s_add_u32 s89, s89, s39
	s_movk_i32 s90, 6
	s_mov_b32 s32, 0
	s_add_u32 s86, s84, 0x9180000
	s_addc_u32 s87, s85, 0
	s_add_u32 s84, s84, 0x1100000
	s_addc_u32 s85, s85, 0
	s_add_u32 s14, s8, 0x900000
	s_addc_u32 s15, s9, 0
	s_add_u32 s16, s8, 0xb00000
	s_addc_u32 s17, s9, 0
	s_add_u32 s18, s8, 0xd00000
	s_addc_u32 s19, s9, 0
	v_mov_b32_e32 v131, 0
	s_add_u32 s20, s8, 0x4000
	v_mov_b32_e32 v133, v131
	s_addc_u32 s21, s9, 0
	v_lshl_add_u64 v[2:3], s[8:9], 0, v[132:133]
	s_mov_b64 s[8:9], 0x1d1c0000
	s_waitcnt vmcnt(0)
	v_lshl_add_u64 v[12:13], v[2:3], 0, s[8:9]
	s_mov_b64 s[8:9], 0x1d1c0100
	s_movk_i32 s4, 0x100
	v_mov_b32_e32 v135, v131
	v_lshl_add_u64 v[14:15], v[2:3], 0, s[8:9]
	s_mov_b64 s[8:9], 0x1d1c0200
	v_cmp_gt_i32_e64 s[4:5], s4, v1
	s_mov_b32 s26, 0
	v_lshl_add_u32 v22, v1, 2, 0
	s_lshl_b32 s27, s49, 5
	v_lshl_add_u64 v[10:11], s[6:7], 0, v[134:135]
	v_cmp_gt_u32_e64 s[6:7], 8, v130
	v_lshl_add_u64 v[16:17], v[2:3], 0, s[8:9]
	v_mov_b64_e32 v[18:19], 0x100
	v_mov_b64_e32 v[20:21], 0xff
	v_mov_b32_e32 v23, 0xff800000
	v_mov_b32_e32 v24, 1
	s_waitcnt vmcnt(0)
	s_barrier
	s_branch .LBB0_532
